# P7/P9/P17: workgroups on odd XCDs start the phase ~7us later so the HBM-bound epilogue bursts of the two halves do not coincide
# baseline (speedup 1.0000x reference)
.LBB0_982:
	s_cmp_gt_i32 s90, 7
	s_cselect_b64 s[0:1], -1, 0
	s_cmp_lt_i32 s91, 8
	s_cselect_b64 s[2:3], -1, 0
	s_or_b64 s[0:1], s[0:1], s[2:3]
	s_and_b64 vcc, exec, s[0:1]
	s_cbranch_vccnz .LBB0_1099
	s_waitcnt vmcnt(0)
	s_bitcmp1_b32 s84, 0
	s_cbranch_scc0 .Lstg7_skip
	s_sleep 127
	s_sleep 127
.Lstg7_skip:
	v_lshrrev_b32_e32 v3, 1, v0
	v_and_b32_e32 v10, 24, v3
	v_lshrrev_b32_e32 v3, 5, v0
	v_lshlrev_b32_e32 v1, 4, v0
	v_and_b32_e32 v2, 32, v0
	v_and_b32_e32 v3, 4, v3
	v_bfe_u32 v4, v0, 2, 2
	s_add_u32 s0, s88, 0x2f400000
	v_bfe_u32 v227, v0, 2, 4
	v_bitop3_b32 v225, v1, v2, 48 bitop3:0x6c
	v_and_b32_e32 v226, 64, v0
	v_or3_b32 v3, v3, v4, v10
	v_lshrrev_b32_e32 v4, 3, v0
	v_or_b32_e32 v228, 0x2000, v1
	s_addc_u32 s1, s89, 0
	v_or_b32_e32 v2, v225, v226
	v_and_or_b32 v5, v4, 48, v227
	v_and_or_b32 v4, v4, 32, v3
	v_lshrrev_b32_e32 v1, 7, v228
	s_movk_i32 s2, 0x70
	v_lshl_or_b32 v198, v4, 11, v2
	v_and_or_b32 v4, v1, s2, v227
	s_movk_i32 s2, 0x60
	s_cmpk_lt_i32 s84, 0x200
	v_and_or_b32 v1, v1, s2, v3
	s_cselect_b64 s[2:3], -1, 0
	s_ashr_i32 s50, s84, 31
	s_lshr_b32 s4, s50, 29
	s_add_i32 s4, s84, s4
	s_ashr_i32 s46, s4, 3
	s_and_b32 s4, s4, -8
	s_ashr_i32 s33, s96, 31
	s_sub_i32 s48, s84, s4
	s_cmp_lt_i32 s48, 0
	v_lshl_or_b32 v196, v5, 11, v2
	v_lshl_or_b32 v200, v4, 11, v2
	v_lshl_or_b32 v202, v1, 11, v2
	v_lshlrev_b32_e32 v1, 6, v0
	v_lshlrev_b32_e32 v2, 2, v0
	s_cselect_b64 s[4:5], -1, 0
	s_lshl_b32 s47, s48, 6
	v_mov_b32_e32 v199, 0
	v_and_b32_e32 v195, 15, v0
	v_and_b32_e32 v1, 0x3c0, v1
	v_and_b32_e32 v224, 32, v2
	s_cmpk_gt_i32 s84, 0x1ff
	v_mov_b32_e32 v203, v199
	v_mov_b32_e32 v197, v199
	v_mov_b32_e32 v201, v199
	s_mulk_i32 s48, 0x41
	v_readfirstlane_b32 s7, v0
	s_cbranch_scc1 .LBB0_1007
	s_add_u32 s49, s88, 0x27400000
	s_addc_u32 s51, s89, 0
	s_add_u32 s52, s88, 0x7c00000
	s_addc_u32 s53, s89, 0
	s_lshr_b32 s16, s7, 6
	s_lshr_b32 s20, s7, 8
	s_lshl_b32 s54, s16, 10
	s_and_b64 s[8:9], s[4:5], exec
	s_cselect_b32 s6, s48, s47
	s_add_i32 s6, s6, s46
	s_ashr_i32 s8, s6, 31
	s_lshr_b32 s8, s8, 25
	s_add_i32 s8, s6, s8
	s_ashr_i32 s9, s8, 7
	s_and_b32 s8, s8, 0xff80
	s_sub_i32 s8, s6, s8
	s_bfe_i32 s6, s8, 0x80000
	s_bfe_u32 s6, s6, 0x3000c
	s_add_i32 s10, s8, s6
	s_bfe_i32 s6, s10, 0x80000
	s_and_b32 s10, s10, 0xf8
	s_sub_i32 s8, s8, s10
	s_lshl_b32 s9, s9, 3
	s_sext_i32_i16 s6, s6
	s_sext_i32_i8 s8, s8
	s_lshr_b32 s6, s6, 3
	s_add_i32 s30, s9, s8
	s_ashr_i32 s31, s30, 31
	s_bfe_i64 s[10:11], s[6:7], 0x100000
	s_lshl_b64 s[8:9], s[30:31], 19
	s_lshl_b64 s[10:11], s[10:11], 19
	s_add_u32 s38, s52, s10
	s_addc_u32 s39, s53, s11
	s_add_i32 s31, s54, 0
	s_add_i32 s55, s31, 0x10000
	s_add_i32 s56, s31, 0x12000
	v_lshl_add_u64 v[2:3], s[38:39], 0, v[198:199]
	s_mov_b32 m0, s55
	s_add_u32 s10, s38, 0x40000
	global_load_lds_dwordx4 v[2:3], off
	v_lshl_add_u64 v[4:5], s[38:39], 0, v[202:203]
	s_mov_b32 m0, s56
	s_addc_u32 s11, s39, 0
	s_add_i32 s57, s31, 0x14000
	s_add_i32 s58, s31, 0x16000
	global_load_lds_dwordx4 v[4:5], off
	v_lshl_add_u64 v[6:7], s[10:11], 0, v[198:199]
	s_mov_b32 m0, s57
	s_add_u32 s34, s49, s8
	global_load_lds_dwordx4 v[6:7], off
	v_lshl_add_u64 v[6:7], s[10:11], 0, v[202:203]
	s_mov_b32 m0, s58
	s_addc_u32 s35, s51, s9
	s_add_i32 s59, s31, 0x2000
	global_load_lds_dwordx4 v[6:7], off
	v_lshl_add_u64 v[8:9], s[34:35], 0, v[196:197]
	s_mov_b32 m0, s31
	s_add_u32 s8, s34, 0x40000
	global_load_lds_dwordx4 v[8:9], off
	v_lshl_add_u64 v[6:7], s[34:35], 0, v[200:201]
	s_mov_b32 m0, s59
	s_addc_u32 s9, s35, 0
	s_add_i32 s60, s31, 0x4000
	global_load_lds_dwordx4 v[6:7], off
	v_lshl_add_u64 v[12:13], s[8:9], 0, v[196:197]
	s_mov_b32 m0, s60
	s_add_i32 s61, s31, 0x6000
	global_load_lds_dwordx4 v[12:13], off
	v_lshl_add_u64 v[12:13], s[8:9], 0, v[200:201]
	s_mov_b32 m0, s61
	s_cmp_eq_u32 s20, 1
	global_load_lds_dwordx4 v[12:13], off
	s_cselect_b64 s[8:9], -1, 0
	s_cmp_lg_u32 s20, 1
	s_cbranch_scc1 .LBB0_986
	s_barrier

.LBB0_1167:
	s_cmp_gt_i32 s90, 9
	s_cselect_b64 s[0:1], -1, 0
	s_cmp_lt_i32 s91, 10
	s_cselect_b64 s[2:3], -1, 0
	s_or_b64 s[0:1], s[0:1], s[2:3]
	s_and_b64 vcc, exec, s[0:1]
	s_cbranch_vccnz .LBB0_1242
	s_cmpk_gt_i32 s84, 0x1ff
	v_readfirstlane_b32 s7, v0
	s_cbranch_scc1 .LBB0_1192
	s_waitcnt vmcnt(0) lgkmcnt(0)
	s_bitcmp1_b32 s84, 0
	s_cbranch_scc0 .Lstg9_skip
	s_sleep 127
	s_sleep 127
.Lstg9_skip:
	v_lshrrev_b32_e32 v3, 1, v0
	v_and_b32_e32 v13, 24, v3
	v_lshrrev_b32_e32 v3, 5, v0
	s_add_u32 s33, s88, 0x2f400000
	v_lshlrev_b32_e32 v1, 4, v0
	v_and_b32_e32 v2, 32, v0
	v_and_b32_e32 v3, 4, v3
	v_bfe_u32 v4, v0, 2, 2
	s_addc_u32 s42, s89, 0
	v_bfe_u32 v12, v0, 2, 4
	v_bitop3_b32 v10, v1, v2, 48 bitop3:0x6c
	v_and_b32_e32 v11, 64, v0
	v_or3_b32 v3, v3, v4, v13
	v_lshrrev_b32_e32 v4, 3, v0
	v_or_b32_e32 v14, 0x2000, v1
	s_add_u32 s43, s88, 0x9c00000
	v_or_b32_e32 v2, v10, v11
	v_and_or_b32 v5, v4, 48, v12
	v_and_or_b32 v4, v4, 32, v3
	v_lshrrev_b32_e32 v1, 7, v14
	s_movk_i32 s0, 0x70
	s_addc_u32 s44, s89, 0
	v_lshl_or_b32 v198, v4, 12, v2
	v_and_or_b32 v4, v1, s0, v12
	s_movk_i32 s0, 0x60
	s_ashr_i32 s46, s84, 31
	v_and_or_b32 v1, v1, s0, v3
	s_lshr_b32 s0, s46, 29
	s_add_i32 s0, s84, s0
	s_and_b32 s1, s0, -8
	s_lshr_b32 s12, s7, 6
	s_sub_i32 s1, s84, s1
	s_lshr_b32 s14, s7, 8
	s_lshl_b32 s45, s12, 10
	s_lshl_b32 s3, s1, 6
	s_ashr_i32 s0, s0, 3
	s_mul_i32 s2, s1, 0x41
	s_cmp_lt_i32 s1, 0
	s_cselect_b32 s1, s2, s3
	s_add_i32 s0, s1, s0
	s_ashr_i32 s1, s0, 31
	s_lshr_b32 s1, s1, 25
	s_add_i32 s1, s0, s1
	s_ashr_i32 s2, s1, 7
	s_and_b32 s1, s1, 0xff80
	s_sub_i32 s0, s0, s1
	s_bfe_i32 s1, s0, 0x80000
	s_bfe_u32 s1, s1, 0x3000c
	s_add_i32 s1, s0, s1
	s_bfe_i32 s3, s1, 0x80000
	s_and_b32 s1, s1, 0xf8
	s_sub_i32 s0, s0, s1
	s_lshl_b32 s2, s2, 3
	s_sext_i32_i16 s3, s3
	s_sext_i32_i8 s0, s0
	s_lshr_b32 s6, s3, 3
	s_add_i32 s26, s2, s0
	s_ashr_i32 s27, s26, 31
	s_bfe_i64 s[2:3], s[6:7], 0x100000
	s_lshl_b64 s[0:1], s[26:27], 20
	s_lshl_b64 s[2:3], s[2:3], 20
	s_add_u32 s34, s43, s2
	s_addc_u32 s35, s44, s3
	s_add_i32 s27, s45, 0
	s_add_i32 s47, s27, 0x10000
	s_add_i32 s48, s27, 0x12000
	s_mov_b32 m0, s47
	s_add_u32 s2, s34, 0x80000
	v_lshl_or_b32 v202, v1, 12, v2
	global_load_lds_dwordx4 v198, s[34:35]
	s_mov_b32 m0, s48
	s_addc_u32 s3, s35, 0
	s_add_i32 s49, s27, 0x14000
	s_add_i32 s50, s27, 0x16000
	global_load_lds_dwordx4 v202, s[34:35]
	s_mov_b32 m0, s49
	s_add_u32 s28, s33, s0
	global_load_lds_dwordx4 v198, s[2:3]
	s_mov_b32 m0, s50
	s_addc_u32 s29, s42, s1
	s_add_i32 s51, s27, 0x2000
	v_lshl_or_b32 v196, v5, 12, v2
	global_load_lds_dwordx4 v202, s[2:3]
	s_mov_b32 m0, s27
	s_add_u32 s0, s28, 0x80000
	v_lshl_or_b32 v200, v4, 12, v2
	global_load_lds_dwordx4 v196, s[28:29]
	s_mov_b32 m0, s51
	s_addc_u32 s1, s29, 0
	s_add_i32 s52, s27, 0x4000
	global_load_lds_dwordx4 v200, s[28:29]
	s_mov_b32 m0, s52
	s_add_i32 s53, s27, 0x6000
	global_load_lds_dwordx4 v196, s[0:1]
	s_mov_b32 m0, s53
	v_mov_b32_e32 v199, 0
	global_load_lds_dwordx4 v200, s[0:1]
	s_load_dwordx2 s[0:1], s[86:87], 0x0
	v_mov_b32_e32 v203, v199
	v_mov_b32_e32 v197, v199
	v_mov_b32_e32 v201, v199
	s_cmp_eq_u32 s14, 1
	s_mov_b32 s30, 0
	v_lshl_add_u64 v[8:9], s[34:35], 0, v[198:199]
	v_lshl_add_u64 v[6:7], s[34:35], 0, v[202:203]
	v_lshl_add_u64 v[2:3], s[28:29], 0, v[196:197]
	s_cselect_b64 s[2:3], -1, 0
	s_cmp_lg_u32 s14, 1
	v_lshl_add_u64 v[4:5], s[28:29], 0, v[200:201]
	s_cbranch_scc1 .LBB0_1171
	s_barrier

.LBB0_1716:
	s_cmp_gt_i32 s90, 17
	s_cselect_b64 s[0:1], -1, 0
	s_cmp_lt_i32 s91, 18
	s_cselect_b64 s[2:3], -1, 0
	s_or_b64 s[0:1], s[0:1], s[2:3]
	s_and_b64 vcc, exec, s[0:1]
	s_cbranch_vccnz .LBB0_1791
	s_cmpk_gt_i32 s84, 0x1ff
	v_readfirstlane_b32 s7, v0
	s_cbranch_scc1 .LBB0_1741
	s_waitcnt vmcnt(0)
	s_bitcmp1_b32 s84, 0
	s_cbranch_scc0 .Lstg17_skip
	s_sleep 127
	s_sleep 127
.Lstg17_skip:
	v_lshrrev_b32_e32 v4, 1, v0
	v_and_b32_e32 v12, 24, v4
	v_lshrrev_b32_e32 v4, 5, v0
	s_add_u32 s33, s88, 0xcc00000
	v_lshlrev_b32_e32 v2, 4, v0
	v_and_b32_e32 v1, 32, v0
	v_and_b32_e32 v4, 4, v4
	v_bfe_u32 v5, v0, 2, 2
	s_addc_u32 s44, s89, 0
	v_bfe_u32 v11, v0, 2, 4
	v_bitop3_b32 v1, v2, v1, 48 bitop3:0x6c
	v_and_b32_e32 v10, 64, v0
	v_or3_b32 v4, v4, v5, v12
	v_lshrrev_b32_e32 v5, 3, v0
	v_or_b32_e32 v13, 0x2000, v2
	s_add_u32 s45, s88, 0x33400000
	s_waitcnt lgkmcnt(0)
	v_or_b32_e32 v3, v1, v10
	v_and_or_b32 v6, v5, 48, v11
	v_and_or_b32 v5, v5, 32, v4
	v_lshrrev_b32_e32 v2, 7, v13
	s_movk_i32 s0, 0x70
	s_addc_u32 s46, s89, 0
	v_lshl_or_b32 v196, v5, 12, v3
	v_and_or_b32 v5, v2, s0, v11
	s_movk_i32 s0, 0x60
	s_ashr_i32 s48, s84, 31
	v_and_or_b32 v2, v2, s0, v4
	s_lshr_b32 s0, s48, 29
	s_add_i32 s0, s84, s0
	s_ashr_i32 s1, s0, 3
	s_and_b32 s0, s0, -8
	s_lshr_b32 s12, s7, 6
	s_sub_i32 s0, s84, s0
	s_lshr_b32 s14, s7, 8
	s_lshl_b32 s47, s12, 10
	s_lshl_b32 s3, s0, 6
	s_mul_i32 s2, s0, 0x41
	s_cmp_lt_i32 s0, 0
	s_cselect_b32 s0, s2, s3
	s_add_i32 s0, s0, s1
	s_ashr_i32 s1, s0, 31
	s_lshr_b32 s1, s1, 25
	s_add_i32 s1, s0, s1
	s_ashr_i32 s2, s1, 7
	s_and_b32 s1, s1, 0xff80
	s_sub_i32 s0, s0, s1
	s_bfe_i32 s1, s0, 0x80000
	s_bfe_u32 s1, s1, 0x3000c
	s_add_i32 s1, s0, s1
	s_bfe_i32 s3, s1, 0x80000
	s_and_b32 s1, s1, 0xf8
	s_sub_i32 s0, s0, s1
	s_lshl_b32 s2, s2, 3
	s_sext_i32_i16 s3, s3
	s_sext_i32_i8 s0, s0
	s_lshr_b32 s6, s3, 3
	s_add_i32 s28, s2, s0
	s_ashr_i32 s29, s28, 31
	s_bfe_i64 s[2:3], s[6:7], 0x100000
	s_lshl_b64 s[0:1], s[28:29], 20
	s_lshl_b64 s[2:3], s[2:3], 20
	s_add_u32 s36, s33, s2
	s_addc_u32 s37, s44, s3
	s_add_i32 s29, s47, 0
	s_add_i32 s49, s29, 0x10000
	s_add_i32 s50, s29, 0x12000
	s_mov_b32 m0, s49
	s_add_u32 s2, s36, 0x80000
	v_lshl_or_b32 v200, v2, 12, v3
	global_load_lds_dwordx4 v196, s[36:37]
	s_mov_b32 m0, s50
	s_addc_u32 s3, s37, 0
	s_add_i32 s51, s29, 0x14000
	s_add_i32 s52, s29, 0x16000
	global_load_lds_dwordx4 v200, s[36:37]
	s_mov_b32 m0, s51
	s_add_u32 s30, s45, s0
	global_load_lds_dwordx4 v196, s[2:3]
	s_mov_b32 m0, s52
	s_addc_u32 s31, s46, s1
	s_add_i32 s53, s29, 0x2000
	v_lshl_or_b32 v192, v6, 12, v3
	global_load_lds_dwordx4 v200, s[2:3]
	s_mov_b32 m0, s29
	s_add_u32 s0, s30, 0x80000
	v_lshl_or_b32 v198, v5, 12, v3
	global_load_lds_dwordx4 v192, s[30:31]
	s_mov_b32 m0, s53
	s_addc_u32 s1, s31, 0
	s_add_i32 s54, s29, 0x4000
	global_load_lds_dwordx4 v198, s[30:31]
	s_mov_b32 m0, s54
	s_add_i32 s55, s29, 0x6000
	global_load_lds_dwordx4 v192, s[0:1]
	s_mov_b32 m0, s55
	v_mov_b32_e32 v197, 0
	global_load_lds_dwordx4 v198, s[0:1]
	v_mov_b32_e32 v201, v197
	v_mov_b32_e32 v193, v197
	v_mov_b32_e32 v199, v197
	s_cmp_eq_u32 s14, 1
	s_mov_b32 s34, 0
	v_lshl_add_u64 v[8:9], s[36:37], 0, v[196:197]
	v_lshl_add_u64 v[6:7], s[36:37], 0, v[200:201]
	v_lshl_add_u64 v[2:3], s[30:31], 0, v[192:193]
	s_cselect_b64 s[0:1], -1, 0
	s_cmp_lg_u32 s14, 1
	v_lshl_add_u64 v[4:5], s[30:31], 0, v[198:199]
	s_cbranch_scc1 .LBB0_1720
	s_barrier
